# P10 boundary-row fix-up: an item's four conditional neighbour-row loads are issued together with its other loads, one wait, then the unpacks under saved condition masks
# baseline (speedup 1.0000x reference)
; __device__ __forceinline__ unsigned pk_bf16(float lo, float hi) { const f32x2 f = {lo, hi}; const bf16v2 r = __builtin_convertvector(f, bf16v2); return __builtin_bit_cast(unsigned, r); }
; #define GAS __attribute__((address_space(1)))
; DI void ffn_fix(const bf16* UB, bf16* ACT, const float* cw, const float* cb, int gt, int NT) {
;     ...
; #pragma unroll
;         for (int hf = 0; hf < 2; ++hf) {
;             const int col = hf * DFF + n0; float x0[8], x1[8], x2[8];
;             ld8(cur + col, x0);
;             if (!z1) ld8(p1 + col, x1); else {
; #pragma unroll
;                 for (int e = 0; e < 8; ++e) x1[e] = 0.f; }
;             if (!z2) ld8(p2 + col, x2); else {
; #pragma unroll
;                 for (int e = 0; e < 8; ++e) x2[e] = 0.f; }
; #pragma unroll
;             for (int e = 0; e < 8; ++e) o[hf][e] = cb[col + e] + cw[col + e] * x2[e] + cw[(size_t)DFF2 + col + e] * x1[e] + cw[2 * (size_t)DFF2 + col + e] * x0[e];
;         }
;         float a[8];
; #pragma unroll
;         for (int e = 0; e < 8; ++e) a[e] = o[0][e] * __builtin_amdgcn_rcpf(1.0f + __expf(-o[0][e])) * o[1][e];
;         v4u ov; ov.x = pk_bf16(a[0], a[1]); ov.y = pk_bf16(a[2], a[3]); ov.z = pk_bf16(a[4], a[5]); ov.w = pk_bf16(a[6], a[7]);
;         *(GAS v4u*)(ACT + pg8::blk_elem(blk * 64 + rho, n0, DFF)) = ov;
.LBB0_1329:
	s_or_b64 exec, exec, s[20:21]
	s_waitcnt vmcnt(0)
	s_and_saveexec_b64 s[20:21], s[98:99]
	v_lshlrev_b32_e32 v46, 16, v120
	v_and_b32_e32 v47, 0xffff0000, v120
	v_lshlrev_b32_e32 v48, 16, v121
	v_and_b32_e32 v49, 0xffff0000, v121
	v_lshlrev_b32_e32 v50, 16, v122
	v_and_b32_e32 v51, 0xffff0000, v122
	v_lshlrev_b32_e32 v52, 16, v123
	v_and_b32_e32 v53, 0xffff0000, v123
	v_lshlrev_b32_e32 v60, 16, v128
	v_and_b32_e32 v61, 0xffff0000, v128
	v_lshlrev_b32_e32 v64, 16, v129
	v_and_b32_e32 v65, 0xffff0000, v129
	v_lshlrev_b32_e32 v68, 16, v130
	v_and_b32_e32 v69, 0xffff0000, v130
	v_lshlrev_b32_e32 v56, 16, v131
	v_and_b32_e32 v57, 0xffff0000, v131
	s_or_b64 exec, exec, s[20:21]
	s_and_saveexec_b64 s[20:21], s[100:101]
	v_lshlrev_b32_e32 v54, 16, v124
	v_and_b32_e32 v55, 0xffff0000, v124
	v_lshlrev_b32_e32 v58, 16, v125
	v_and_b32_e32 v59, 0xffff0000, v125
	v_lshlrev_b32_e32 v62, 16, v126
	v_and_b32_e32 v63, 0xffff0000, v126
	v_lshlrev_b32_e32 v66, 16, v127
	v_and_b32_e32 v67, 0xffff0000, v127
	v_lshlrev_b32_e32 v70, 16, v132
	v_and_b32_e32 v71, 0xffff0000, v132
	v_lshlrev_b32_e32 v74, 16, v133
	v_and_b32_e32 v75, 0xffff0000, v133
	v_lshlrev_b32_e32 v76, 16, v134
	v_and_b32_e32 v77, 0xffff0000, v134
	v_lshlrev_b32_e32 v72, 16, v135
	v_and_b32_e32 v73, 0xffff0000, v135
	s_or_b64 exec, exec, s[20:21]
	v_readlane_b32 s36, v254, 2
	v_readlane_b32 s40, v254, 6
	v_readlane_b32 s41, v254, 7
	v_readlane_b32 s42, v254, 8
	v_readlane_b32 s43, v254, 9
	s_mov_b64 s[20:21], s[40:41]
	v_lshlrev_b64 v[78:79], 2, v[42:43]
	s_mov_b64 s[22:23], s[42:43]
	v_lshl_add_u64 v[112:113], s[20:21], 0, v[78:79]
	v_lshl_add_u64 v[78:79], s[22:23], 0, v[78:79]
	global_load_dwordx4 v[84:87], v[78:79], off offset:16
	global_load_dwordx4 v[88:91], v[78:79], off
	global_load_dwordx4 v[92:95], v[112:113], off offset:16
	global_load_dwordx4 v[96:99], v[112:113], off
	v_add_co_u32_e32 v78, vcc, s26, v112
	v_lshl_add_u64 v[108:109], v[112:113], 0, s[16:17]
	s_nop 0
	v_addc_co_u32_e32 v79, vcc, 0, v113, vcc
	global_load_dwordx4 v[100:103], v[78:79], off offset:2048
	global_load_dwordx4 v[104:107], v[108:109], off offset:16
	v_add_co_u32_e32 v78, vcc, s25, v112
	s_waitcnt vmcnt(11)
	v_pk_fma_f32 v[22:23], v[54:55], v[30:31], v[22:23]
	v_addc_co_u32_e32 v79, vcc, 0, v113, vcc
	global_load_dwordx4 v[108:111], v[78:79], off
	v_lshl_add_u64 v[78:79], v[112:113], 0, s[18:19]
	global_load_dwordx4 v[112:115], v[78:79], off offset:16
	v_pk_fma_f32 v[24:25], v[58:59], v[32:33], v[24:25]
	v_lshlrev_b32_e32 v78, 16, v2
	v_and_b32_e32 v79, 0xffff0000, v2
	v_lshlrev_b32_e32 v2, 16, v3
	v_and_b32_e32 v3, 0xffff0000, v3
	v_pk_fma_f32 v[6:7], v[62:63], v[10:11], v[6:7]
	v_pk_fma_f32 v[8:9], v[66:67], v[12:13], v[8:9]
	s_waitcnt vmcnt(12)
	v_pk_fma_f32 v[22:23], v[46:47], v[26:27], v[22:23]
	v_pk_fma_f32 v[24:25], v[48:49], v[28:29], v[24:25]
	v_lshlrev_b32_e32 v116, 16, v4
	v_and_b32_e32 v117, 0xffff0000, v4
	v_lshlrev_b32_e32 v4, 16, v5
	v_and_b32_e32 v5, 0xffff0000, v5
	s_waitcnt vmcnt(10)
	v_pk_fma_f32 v[6:7], v[50:51], v[34:35], v[6:7]
	v_pk_fma_f32 v[8:9], v[52:53], v[36:37], v[8:9]
	v_pk_fma_f32 v[18:19], v[18:19], v[78:79], v[22:23]
	v_pk_fma_f32 v[2:3], v[20:21], v[2:3], v[24:25]
	s_waitcnt vmcnt(9)
	v_pk_fma_f32 v[6:7], v[14:15], v[116:117], v[6:7]
	v_pk_fma_f32 v[4:5], v[16:17], v[4:5], v[8:9]
	v_mul_f32_e32 v8, 0xbfb8aa3b, v18
	v_mul_f32_e32 v9, 0xbfb8aa3b, v19
	v_mul_f32_e32 v14, 0xbfb8aa3b, v2
	v_mul_f32_e32 v15, 0xbfb8aa3b, v3
	v_exp_f32_e32 v8, v8
	v_exp_f32_e32 v9, v9
	v_exp_f32_e32 v14, v14
	v_exp_f32_e32 v15, v15
	v_add_f32_e32 v8, 1.0, v8
	v_add_f32_e32 v9, 1.0, v9
	v_add_f32_e32 v14, 1.0, v14
	v_add_f32_e32 v15, 1.0, v15
	v_rcp_f32_e32 v8, v8
	v_rcp_f32_e32 v9, v9
	v_rcp_f32_e32 v14, v14
	v_rcp_f32_e32 v15, v15
	v_mul_f32_e32 v16, 0xbfb8aa3b, v6
	v_mul_f32_e32 v17, 0xbfb8aa3b, v7
	v_exp_f32_e32 v16, v16
	v_exp_f32_e32 v17, v17
	v_pk_mul_f32 v[8:9], v[18:19], v[8:9]
	v_pk_mul_f32 v[2:3], v[2:3], v[14:15]
	s_waitcnt vmcnt(8)
	v_lshlrev_b32_e32 v10, 16, v38
	v_and_b32_e32 v11, 0xffff0000, v38
	v_lshlrev_b32_e32 v12, 16, v39
	v_and_b32_e32 v13, 0xffff0000, v39
	v_add_f32_e32 v16, 1.0, v16
	v_add_f32_e32 v17, 1.0, v17
	v_rcp_f32_e32 v16, v16
	v_rcp_f32_e32 v17, v17
	v_lshlrev_b32_e32 v30, 16, v40
	v_and_b32_e32 v31, 0xffff0000, v40
	v_lshlrev_b32_e32 v32, 16, v41
	v_pk_mul_f32 v[6:7], v[6:7], v[16:17]
	v_and_b32_e32 v33, 0xffff0000, v41
	v_sub_u32_e32 v38, v208, v82
	v_add_u32_e32 v208, s72, v208
	v_cmp_lt_i32_e32 vcc, s28, v208
	s_or_b64 s[12:13], vcc, s[12:13]
	v_add_u32_e32 v1, s3, v1
	v_readlane_b32 s37, v254, 3
	v_readlane_b32 s38, v254, 4
	v_readlane_b32 s39, v254, 5
	s_waitcnt vmcnt(5)
	v_pk_fma_f32 v[20:21], v[76:77], v[92:93], v[84:85]
	s_waitcnt vmcnt(4)
	v_pk_fma_f32 v[14:15], v[70:71], v[96:97], v[88:89]
	v_pk_fma_f32 v[18:19], v[74:75], v[98:99], v[90:91]
	s_waitcnt vmcnt(3)
	v_pk_fma_f32 v[14:15], v[60:61], v[100:101], v[14:15]
	v_pk_fma_f32 v[18:19], v[64:65], v[102:103], v[18:19]
	s_waitcnt vmcnt(2)
	v_pk_fma_f32 v[20:21], v[68:69], v[104:105], v[20:21]
	s_waitcnt vmcnt(1)
	v_pk_fma_f32 v[10:11], v[108:109], v[10:11], v[14:15]
	v_pk_fma_f32 v[12:13], v[110:111], v[12:13], v[18:19]
	v_pk_mul_f32 v[8:9], v[8:9], v[10:11]
	v_pk_mul_f32 v[10:11], v[2:3], v[12:13]
	v_mul_f32_e32 v12, 0xbfb8aa3b, v4
	v_mul_f32_e32 v13, 0xbfb8aa3b, v5
	v_exp_f32_e32 v12, v12
	v_exp_f32_e32 v13, v13
	s_waitcnt vmcnt(0)
	v_pk_fma_f32 v[2:3], v[112:113], v[30:31], v[20:21]
	s_nop 0
	v_pk_mul_f32 v[6:7], v[6:7], v[2:3]
	v_add_f32_e32 v2, 1.0, v12
	v_add_f32_e32 v3, 1.0, v13
	v_rcp_f32_e32 v2, v2
	v_rcp_f32_e32 v3, v3
	v_pk_fma_f32 v[12:13], v[72:73], v[94:95], v[86:87]
	v_pk_mul_f32 v[2:3], v[4:5], v[2:3]
	v_pk_fma_f32 v[12:13], v[56:57], v[106:107], v[12:13]
	v_cvt_pk_bf16_f32 v4, v6, v7
	v_pk_fma_f32 v[12:13], v[114:115], v[32:33], v[12:13]
	v_lshrrev_b32_e32 v6, 3, v80
	v_pk_mul_f32 v[12:13], v[2:3], v[12:13]
	v_cvt_pk_bf16_f32 v2, v8, v9
	v_ashrrev_i32_e32 v7, 3, v38
	v_lshlrev_b32_e32 v9, 3, v81
	v_cvt_pk_bf16_f32 v3, v10, v11
	v_mad_i32_i24 v6, v6, s27, v7
	v_and_b32_e32 v9, 8, v9
	v_lshrrev_b32_e32 v10, 5, v44
	v_lshlrev_b32_e32 v11, 1, v44
	v_ashrrev_i32_e32 v7, 31, v6
	v_lshlrev_b32_e32 v8, 13, v81
	v_and_or_b32 v9, v10, 1, v9
	v_lshlrev_b32_e32 v10, 6, v80
	v_and_b32_e32 v11, 48, v11
	v_lshlrev_b64 v[6:7], 15, v[6:7]
	v_and_b32_e32 v8, 0x4000, v8
	v_and_or_b32 v10, v10, 64, v11
	v_lshlrev_b32_e32 v9, 10, v9
	v_or3_b32 v42, v10, v9, v8
	v_lshl_add_u64 v[6:7], s[10:11], 0, v[6:7]
	v_cvt_pk_bf16_f32 v5, v12, v13
	v_lshl_add_u64 v[6:7], v[6:7], 0, v[42:43]
	global_store_dwordx4 v[6:7], v[2:5], off
	s_andn2_b64 exec, exec, s[12:13]
	s_cbranch_execz .LBB0_1342
; DI void ffn_fix(const bf16* UB, bf16* ACT, const float* cw, const float* cb, int gt, int NT) {
;     ...
;     for (int it = gt; it < (M / 64) * 2 * NC; it += NT) {
;         const int cc = it % NC, rr = it / NC, rho = rr & 1, blk = rr >> 1, n0 = 8 * cc; const bool first = (blk & 127) == 0;
;         const bf16* cur = UB + ((size_t)blk * 4 + rho) * DFF2; const bf16* prv = UB + ((size_t)(blk - 1) * 4) * DFF2;
;         const bf16* p1 = rho ? UB + ((size_t)blk * 4) * DFF2 : prv + 3 * (size_t)DFF2;
;         const bf16* p2 = rho ? prv + 3 * (size_t)DFF2 : prv + 2 * (size_t)DFF2;
;         const bool z1 = (rho == 0) && first, z2 = first;
;         float o[2][8];
; #pragma unroll
;         for (int hf = 0; hf < 2; ++hf) {
;             const int col = hf * DFF + n0; float x0[8], x1[8], x2[8];
;             ld8(cur + col, x0);
;             if (!z1) ld8(p1 + col, x1); else {
; #pragma unroll
;                 for (int e = 0; e < 8; ++e) x1[e] = 0.f; }
;             if (!z2) ld8(p2 + col, x2); else {
; #pragma unroll
;                 for (int e = 0; e < 8; ++e) x2[e] = 0.f; }
.LBB0_1330:
	v_mul_hi_i32 v2, v208, s24
	s_waitcnt lgkmcnt(0)
	v_lshrrev_b32_e32 v3, 31, v2
	v_ashrrev_i32_e32 v2, 8, v2
	v_add_u32_e32 v80, v2, v3
	v_and_b32_e32 v2, 1, v80
	v_ashrrev_i32_e32 v81, 1, v80
	v_cmp_eq_u32_e32 vcc, 1, v2
	s_and_saveexec_b64 s[0:1], vcc
	s_xor_b64 s[0:1], exec, s[0:1]
	v_mul_hi_i32_i24_e32 v5, 0x2b000, v81
	v_mul_i32_i24_e32 v4, 0x2b000, v81
	v_lshl_add_u64 v[72:73], s[8:9], 0, v[4:5]
	s_or_saveexec_b64 s[0:1], s[0:1]
	v_add_u32_e32 v3, -1, v81
	v_mul_hi_i32_i24_e32 v5, 0x2b000, v3
	v_mul_i32_i24_e32 v4, 0x2b000, v3
	v_lshl_add_u64 v[6:7], s[8:9], 0, v[4:5]
	v_mov_b64_e32 v[8:9], 0x20400
	s_xor_b64 exec, exec, s[0:1]
	v_lshl_add_u64 v[72:73], v[6:7], 0, s[14:15]
	v_mov_b64_e32 v[8:9], 0x15800
	s_or_b64 exec, exec, s[0:1]
	v_mul_i32_i24_e32 v82, 0x560, v80
	v_lshlrev_b32_e32 v3, 3, v82
	v_lshl_or_b32 v2, v81, 2, v2
	v_sub_u32_e32 v44, v1, v3
	v_mul_hi_i32_i24_e32 v3, 0xac00, v2
	v_mul_i32_i24_e32 v2, 0xac00, v2
	v_lshl_add_u64 v[38:39], s[8:9], 0, v[2:3]
	v_ashrrev_i32_e32 v45, 31, v44
	v_lshl_add_u64 v[2:3], v[44:45], 1, v[38:39]
	global_load_dwordx4 v[2:5], v[2:3], off
	v_cmp_ne_u32_sdwa s[20:21], v80, v43 src0_sel:BYTE_0 src1_sel:DWORD
	v_mov_b32_e32 v54, 0
	v_mov_b32_e32 v46, 0
	v_mov_b32_e32 v47, 0
	v_mov_b32_e32 v48, 0
	v_mov_b32_e32 v49, 0
	v_mov_b32_e32 v50, 0
	v_mov_b32_e32 v51, 0
	v_mov_b32_e32 v52, 0
	v_mov_b32_e32 v53, 0
	s_mov_b64 s[98:99], s[20:21]
	s_and_saveexec_b64 s[0:1], s[20:21]
	s_cbranch_execz .LBB0_1336
	v_lshl_add_u64 v[10:11], v[44:45], 1, v[72:73]
	global_load_dwordx4 v[120:123], v[10:11], off
.LBB0_1336:
	s_or_b64 exec, exec, s[0:1]
	v_lshl_add_u64 v[78:79], v[6:7], 0, v[8:9]
	v_and_b32_e32 v6, 0xfe, v80
	v_cmp_ne_u32_e64 s[0:1], 0, v6
	v_mov_b32_e32 v55, 0
	v_mov_b32_e32 v58, 0
	v_mov_b32_e32 v59, 0
	v_mov_b32_e32 v62, 0
	v_mov_b32_e32 v63, 0
	v_mov_b32_e32 v66, 0
	v_mov_b32_e32 v67, 0
	s_mov_b64 s[100:101], s[0:1]
	s_and_saveexec_b64 s[22:23], s[0:1]
	s_cbranch_execz .LBB0_1338
	v_lshl_add_u64 v[6:7], v[44:45], 1, v[78:79]
	global_load_dwordx4 v[124:127], v[6:7], off
.LBB0_1338:
	s_or_b64 exec, exec, s[22:23]
	v_readlane_b32 s36, v254, 2
	v_lshlrev_b64 v[6:7], 2, v[44:45]
	v_readlane_b32 s40, v254, 6
	v_readlane_b32 s41, v254, 7
	v_readlane_b32 s42, v254, 8
	v_readlane_b32 s43, v254, 9
	v_lshl_add_u64 v[14:15], s[40:41], 0, v[6:7]
	v_lshl_add_u64 v[40:41], v[14:15], 0, s[16:17]
	v_lshl_add_u64 v[16:17], s[42:43], 0, v[6:7]
	global_load_dwordx4 v[6:9], v[16:17], off offset:16
	global_load_dwordx4 v[22:25], v[16:17], off
	global_load_dwordx4 v[10:13], v[14:15], off offset:16
	global_load_dwordx4 v[30:33], v[14:15], off
	v_add_co_u32_e32 v16, vcc, 0x15000, v14
	v_lshl_add_u64 v[56:57], v[14:15], 0, s[18:19]
	s_nop 0
	v_addc_co_u32_e32 v17, vcc, 0, v15, vcc
	v_add_co_u32_e32 v60, vcc, 0x2b000, v14
	v_add_u32_e32 v42, 0x2b00, v44
	s_nop 0
	v_addc_co_u32_e32 v61, vcc, 0, v15, vcc
	global_load_dwordx4 v[26:29], v[16:17], off offset:2048
	global_load_dwordx4 v[18:21], v[60:61], off
	global_load_dwordx4 v[34:37], v[40:41], off offset:16
	s_nop 0
	global_load_dwordx4 v[14:17], v[56:57], off offset:16
	v_lshl_add_u64 v[38:39], v[42:43], 1, v[38:39]
	global_load_dwordx4 v[38:41], v[38:39], off
	v_mov_b32_e32 v70, 0
	v_mov_b32_e32 v60, 0
	v_mov_b32_e32 v61, 0
	v_mov_b32_e32 v64, 0
	v_mov_b32_e32 v65, 0
	v_mov_b32_e32 v68, 0
	v_mov_b32_e32 v69, 0
	v_mov_b32_e32 v56, 0
	v_mov_b32_e32 v57, 0
	v_readlane_b32 s37, v254, 3
	v_readlane_b32 s38, v254, 4
	v_readlane_b32 s39, v254, 5
	s_and_saveexec_b64 s[22:23], s[20:21]
	s_cbranch_execz .LBB0_1340
	v_lshl_add_u64 v[56:57], v[42:43], 1, v[72:73]
	global_load_dwordx4 v[128:131], v[56:57], off
.LBB0_1340:
	s_or_b64 exec, exec, s[22:23]
	v_mov_b32_e32 v71, 0
	v_mov_b32_e32 v74, 0
	v_mov_b32_e32 v75, 0
	v_mov_b32_e32 v76, 0
	v_mov_b32_e32 v77, 0
	v_mov_b32_e32 v72, 0
	v_mov_b32_e32 v73, 0
	s_and_saveexec_b64 s[20:21], s[0:1]
	s_cbranch_execz .LBB0_1329
	v_lshl_add_u64 v[70:71], v[42:43], 1, v[78:79]
	global_load_dwordx4 v[132:135], v[70:71], off
	s_branch .LBB0_1329
